# GEMM K-loop header: drop compiler's lgkmcnt(0) between B and A fragment reads (16 reads in flight)
# speedup vs baseline: 1.0305x; 1.0010x over previous
.LBB0_145:
	v_add_u32_e32 v136, 0, v243
	v_add_u32_e32 v137, 0x10000, v136
	v_add_u32_e32 v148, 0x14000, v136
	ds_read_b128 v[152:155], v137
	ds_read_b128 v[156:159], v137 offset:1024
	ds_read_b128 v[160:163], v137 offset:2048
	ds_read_b128 v[164:167], v137 offset:3072
	ds_read_b128 v[136:139], v148
	ds_read_b128 v[140:143], v148 offset:1024
	ds_read_b128 v[144:147], v148 offset:2048
	ds_read_b128 v[148:151], v148 offset:3072
	s_cmp_eq_u32 s62, 28
	s_cselect_b64 s[38:39], -1, 0
	s_add_i32 m0, s47, 0xc000
	ds_read_b128 v[192:195], v244
	ds_read_b128 v[196:199], v244 offset:1024
	ds_read_b128 v[184:187], v244 offset:2048
	ds_read_b128 v[188:191], v244 offset:3072
	ds_read_b128 v[176:179], v244 offset:4096
	ds_read_b128 v[180:183], v244 offset:5120
	ds_read_b128 v[168:171], v244 offset:6144
	ds_read_b128 v[172:175], v244 offset:7168
	global_load_lds_dwordx4 v212, s[14:15]
	s_add_i32 m0, s47, 0xe000
	s_and_b64 s[40:41], s[2:3], s[38:39]
	global_load_lds_dwordx4 v216, s[14:15]
	s_andn2_b64 vcc, exec, s[40:41]
	s_cbranch_vccz .LBB0_143
	v_mov_b32_e32 v213, v3
	v_mov_b32_e32 v217, v3
	v_mov_b64_e32 v[224:225], v[216:217]
	v_mov_b64_e32 v[226:227], v[212:213]
	s_branch .LBB0_144

.LBB0_295:
	v_add_u32_e32 v136, 0, v243
	v_add_u32_e32 v137, 0x10000, v136
	v_add_u32_e32 v148, 0x14000, v136
	ds_read_b128 v[152:155], v137
	ds_read_b128 v[156:159], v137 offset:1024
	ds_read_b128 v[160:163], v137 offset:2048
	ds_read_b128 v[164:167], v137 offset:3072
	ds_read_b128 v[136:139], v148
	ds_read_b128 v[140:143], v148 offset:1024
	ds_read_b128 v[144:147], v148 offset:2048
	ds_read_b128 v[148:151], v148 offset:3072
	s_cmp_eq_u32 s61, 28
	s_cselect_b64 s[38:39], -1, 0
	s_add_i32 m0, s45, 0xc000
	ds_read_b128 v[192:195], v244
	ds_read_b128 v[196:199], v244 offset:1024
	ds_read_b128 v[184:187], v244 offset:2048
	ds_read_b128 v[188:191], v244 offset:3072
	ds_read_b128 v[176:179], v244 offset:4096
	ds_read_b128 v[180:183], v244 offset:5120
	ds_read_b128 v[168:171], v244 offset:6144
	ds_read_b128 v[172:175], v244 offset:7168
	global_load_lds_dwordx4 v212, s[14:15]
	s_add_i32 m0, s45, 0xe000
	s_and_b64 s[40:41], s[2:3], s[38:39]
	global_load_lds_dwordx4 v216, s[14:15]
	s_andn2_b64 vcc, exec, s[40:41]
	s_cbranch_vccz .LBB0_293
	v_mov_b32_e32 v213, v3
	v_mov_b32_e32 v217, v3
	v_mov_b64_e32 v[224:225], v[216:217]
	v_mov_b64_e32 v[226:227], v[212:213]
	s_branch .LBB0_294

.LBB0_499:
	v_add_u32_e32 v136, 0, v241
	v_add_u32_e32 v137, 0x10000, v136
	v_add_u32_e32 v148, 0x14000, v136
	ds_read_b128 v[152:155], v137
	ds_read_b128 v[156:159], v137 offset:1024
	ds_read_b128 v[160:163], v137 offset:2048
	ds_read_b128 v[164:167], v137 offset:3072
	ds_read_b128 v[136:139], v148
	ds_read_b128 v[140:143], v148 offset:1024
	ds_read_b128 v[144:147], v148 offset:2048
	ds_read_b128 v[148:151], v148 offset:3072
	s_cmp_eq_u32 s63, 28
	s_cselect_b64 s[14:15], -1, 0
	s_add_i32 m0, s43, 0xc000
	ds_read_b128 v[192:195], v243
	ds_read_b128 v[196:199], v243 offset:1024
	ds_read_b128 v[184:187], v243 offset:2048
	ds_read_b128 v[188:191], v243 offset:3072
	ds_read_b128 v[176:179], v243 offset:4096
	ds_read_b128 v[180:183], v243 offset:5120
	ds_read_b128 v[168:171], v243 offset:6144
	ds_read_b128 v[172:175], v243 offset:7168
	global_load_lds_dwordx4 v212, s[12:13]
	s_add_i32 m0, s43, 0xe000
	s_and_b64 s[38:39], s[2:3], s[14:15]
	global_load_lds_dwordx4 v216, s[12:13]
	s_andn2_b64 vcc, exec, s[38:39]
	s_cbranch_vccz .LBB0_497
	v_mov_b32_e32 v213, v3
	v_mov_b32_e32 v217, v3
	v_mov_b64_e32 v[222:223], v[216:217]
	v_mov_b64_e32 v[224:225], v[212:213]
	s_branch .LBB0_498

.LBB0_1165:
	v_add_u32_e32 v136, 0x10000, v224
	v_add_u32_e32 v148, 0x14000, v224
	ds_read_b128 v[152:155], v136
	ds_read_b128 v[156:159], v136 offset:1024
	ds_read_b128 v[160:163], v136 offset:2048
	ds_read_b128 v[164:167], v136 offset:3072
	ds_read_b128 v[136:139], v148
	ds_read_b128 v[140:143], v148 offset:1024
	ds_read_b128 v[144:147], v148 offset:2048
	ds_read_b128 v[148:151], v148 offset:3072
	s_cmp_eq_u32 s82, 28
	s_cselect_b64 s[54:55], -1, 0
	s_add_i32 m0, s9, 0xc000
	ds_read_b128 v[180:183], v225
	ds_read_b128 v[196:199], v225 offset:1024
	ds_read_b128 v[176:179], v225 offset:2048
	ds_read_b128 v[192:195], v225 offset:3072
	ds_read_b128 v[172:175], v225 offset:4096
	ds_read_b128 v[188:191], v225 offset:5120
	ds_read_b128 v[168:171], v225 offset:6144
	ds_read_b128 v[184:187], v225 offset:7168
	global_load_lds_dwordx4 v218, s[52:53]
	s_add_i32 m0, s9, 0xe000
	s_and_b64 s[4:5], s[50:51], s[54:55]
	global_load_lds_dwordx4 v220, s[52:53]
	s_andn2_b64 vcc, exec, s[4:5]
	s_cbranch_vccnz .LBB0_1175
	ds_read_b32 v2, v227 offset:640
	s_waitcnt lgkmcnt(0)
	v_cmp_gt_i32_e32 vcc, 0, v2
	s_and_saveexec_b64 s[4:5], vcc
	v_mov_b32_e32 v2, s43
	ds_read_b32 v2, v2 offset:640
	s_or_b64 exec, exec, s[4:5]
	ds_read_b32 v213, v227 offset:1152
	s_waitcnt lgkmcnt(0)
	v_cmp_gt_i32_e32 vcc, 0, v213
	s_and_saveexec_b64 s[4:5], vcc
	v_mov_b32_e32 v200, s43
	ds_read_b32 v213, v200 offset:640
	s_or_b64 exec, exec, s[4:5]
	ds_read_b32 v212, v239 offset:640
	s_waitcnt lgkmcnt(0)
	v_cmp_gt_i32_e32 vcc, 0, v212
	s_and_saveexec_b64 s[4:5], vcc
	v_mov_b32_e32 v200, s43
	ds_read_b32 v212, v200 offset:640
	s_or_b64 exec, exec, s[4:5]
	ds_read_b32 v220, v239 offset:1152
	s_waitcnt lgkmcnt(0)
	v_cmp_gt_i32_e32 vcc, 0, v220
	s_and_saveexec_b64 s[4:5], vcc
	v_mov_b32_e32 v200, s43
	ds_read_b32 v220, v200 offset:640
	s_or_b64 exec, exec, s[4:5]
	v_lshlrev_b32_e32 v200, 10, v212
	v_and_b32_e32 v200, 0x7ffff800, v200
	v_add_lshl_u32 v212, v200, v216, 1
	v_lshlrev_b32_e32 v200, 10, v213
	v_and_b32_e32 v200, 0x7ffff800, v200
	v_add_lshl_u32 v218, v200, v217, 1
	v_lshlrev_b32_e32 v2, 10, v2
	s_waitcnt lgkmcnt(0)
	v_lshlrev_b32_e32 v200, 10, v220
	v_and_b32_e32 v2, 0x7ffff800, v2
	v_and_b32_e32 v200, 0x7ffff800, v200
	v_add_lshl_u32 v2, v2, v217, 1
	v_add_lshl_u32 v220, v200, v216, 1

.LBB0_1309:
	v_add_u32_e32 v136, 0x10000, v241
	v_add_u32_e32 v148, 0x14000, v241
	ds_read_b128 v[152:155], v136
	ds_read_b128 v[156:159], v136 offset:1024
	ds_read_b128 v[160:163], v136 offset:2048
	ds_read_b128 v[164:167], v136 offset:3072
	ds_read_b128 v[136:139], v148
	ds_read_b128 v[140:143], v148 offset:1024
	ds_read_b128 v[144:147], v148 offset:2048
	ds_read_b128 v[148:151], v148 offset:3072
	s_cmp_eq_u32 s84, 4
	s_cselect_b64 s[54:55], -1, 0
	s_add_i32 m0, s11, 0xc000
	ds_read_b128 v[180:183], v242
	ds_read_b128 v[196:199], v242 offset:1024
	ds_read_b128 v[176:179], v242 offset:2048
	ds_read_b128 v[192:195], v242 offset:3072
	ds_read_b128 v[172:175], v242 offset:4096
	ds_read_b128 v[188:191], v242 offset:5120
	ds_read_b128 v[168:171], v242 offset:6144
	ds_read_b128 v[184:187], v242 offset:7168
	global_load_lds_dwordx4 v218, s[52:53]
	s_add_i32 m0, s11, 0xe000
	s_and_b64 s[4:5], s[50:51], s[54:55]
	global_load_lds_dwordx4 v219, s[52:53]
	s_andn2_b64 vcc, exec, s[4:5]
	s_cbranch_vccnz .LBB0_1311
	v_mov_b32_e32 v212, v247
	v_mov_b32_e32 v2, v245
	v_mov_b32_e32 v219, v248
	v_mov_b32_e32 v218, v246

.LBB0_1425:
	v_add_u32_e32 v136, 0x10000, v241
	v_add_u32_e32 v148, 0x14000, v241
	ds_read_b128 v[152:155], v136
	ds_read_b128 v[156:159], v136 offset:1024
	ds_read_b128 v[160:163], v136 offset:2048
	ds_read_b128 v[164:167], v136 offset:3072
	ds_read_b128 v[136:139], v148
	ds_read_b128 v[140:143], v148 offset:1024
	ds_read_b128 v[144:147], v148 offset:2048
	ds_read_b128 v[148:151], v148 offset:3072
	s_cmp_eq_u32 s75, 4
	s_cselect_b64 s[50:51], -1, 0
	s_add_i32 m0, s7, 0xc000
	ds_read_b128 v[180:183], v242
	ds_read_b128 v[196:199], v242 offset:1024
	ds_read_b128 v[176:179], v242 offset:2048
	ds_read_b128 v[192:195], v242 offset:3072
	ds_read_b128 v[172:175], v242 offset:4096
	ds_read_b128 v[188:191], v242 offset:5120
	ds_read_b128 v[168:171], v242 offset:6144
	ds_read_b128 v[184:187], v242 offset:7168
	global_load_lds_dwordx4 v218, s[48:49]
	s_add_i32 m0, s7, 0xe000
	s_and_b64 s[4:5], s[44:45], s[50:51]
	global_load_lds_dwordx4 v219, s[48:49]
	s_andn2_b64 vcc, exec, s[4:5]
	s_cbranch_vccnz .LBB0_1427
	v_mov_b32_e32 v212, v247
	v_mov_b32_e32 v2, v245
	v_mov_b32_e32 v219, v248
	v_mov_b32_e32 v218, v246
